# v039 with the MLA -mhat splat spread one instruction per MFMA gap over the P.V slots
# speedup vs baseline: 1.0050x; 1.0050x over previous
; #define PK4(P, BASE, OUT) do { u32x4 w = {cvtpk(P[BASE + 0], P[BASE + 1]), cvtpk(P[BASE + 2], P[BASE + 3]), cvtpk(P[BASE + 4], P[BASE + 5]), cvtpk(P[BASE + 6], P[BASE + 7])}; \
;     OUT = *reinterpret_cast<bf16x8*>(&w); } while (0)
; __device__ __forceinline__ void smax_tile(f32x16& p0, f32x16& p1, float& mhat, float& l_reg, f32x16 (&o)[4], float* al_l, const bool first, int r32, int hi,
;                                           bf16x8& pa0, bf16x8& pa1, bf16x8& pa2, bf16x8& pa3) {
;     ...
; #pragma unroll
;     for (int r = 0; r < 16; ++r) p0[r] = __builtin_amdgcn_exp2f(p0[r]);
; #pragma unroll
;     for (int r = 0; r < 16; ++r) p1[r] = __builtin_amdgcn_exp2f(p1[r]);
;     float ps = p0[0];
; #pragma unroll
;     for (int r = 1; r < 16; ++r) ps += p0[r];
; #pragma unroll
;     for (int r = 0; r < 16; ++r) ps += p1[r];
;     { auto rr = __builtin_amdgcn_permlane32_swap(__float_as_uint(ps), __float_as_uint(ps), false, false); ps = __uint_as_float(rr[0]) + __uint_as_float(rr[1]); }
;     l_reg += ps;
;     ...
;     PK4(p0, 0, pa0); PK4(p0, 8, pa1); PK4(p1, 0, pa2); PK4(p1, 8, pa3);
.LBB0_605:
	v_exp_f32_e32 v96, v96
	v_exp_f32_e32 v97, v97
	v_exp_f32_e32 v98, v98
	v_exp_f32_e32 v99, v99
	v_exp_f32_e32 v100, v100
	v_exp_f32_e32 v101, v101
	v_add_f32_e32 v160, v96, v97
	v_exp_f32_e32 v102, v102
	v_add_f32_e32 v160, v98, v160
	v_exp_f32_e32 v103, v103
	v_add_f32_e32 v160, v99, v160
	v_exp_f32_e32 v104, v104
	v_add_f32_e32 v160, v100, v160
	v_exp_f32_e32 v105, v105
	v_add_f32_e32 v160, v101, v160
	v_exp_f32_e32 v106, v106
	v_add_f32_e32 v160, v102, v160
	v_exp_f32_e32 v107, v107
	v_add_f32_e32 v160, v103, v160
	v_exp_f32_e32 v108, v108
	v_add_f32_e32 v160, v104, v160
	v_exp_f32_e32 v109, v109
	v_add_f32_e32 v160, v105, v160
	v_exp_f32_e32 v110, v110
	v_add_f32_e32 v160, v106, v160
	v_exp_f32_e32 v111, v111
	v_add_f32_e32 v160, v107, v160
	v_exp_f32_e32 v80, v80
	v_add_f32_e32 v160, v108, v160
	v_exp_f32_e32 v81, v81
	v_add_f32_e32 v160, v109, v160
	v_exp_f32_e32 v82, v82
	v_add_f32_e32 v160, v110, v160
	v_exp_f32_e32 v83, v83
	v_add_f32_e32 v160, v111, v160
	v_exp_f32_e32 v84, v84
	v_add_f32_e32 v160, v80, v160
	v_exp_f32_e32 v85, v85
	v_add_f32_e32 v160, v81, v160
	v_exp_f32_e32 v86, v86
	v_add_f32_e32 v160, v82, v160
	v_exp_f32_e32 v87, v87
	v_add_f32_e32 v160, v83, v160
	v_exp_f32_e32 v88, v88
	v_add_f32_e32 v160, v84, v160
	v_exp_f32_e32 v89, v89
	v_add_f32_e32 v160, v85, v160
	v_exp_f32_e32 v90, v90
	v_add_f32_e32 v160, v86, v160
	v_exp_f32_e32 v91, v91
	v_add_f32_e32 v160, v87, v160
	v_exp_f32_e32 v92, v92
	v_add_f32_e32 v160, v88, v160
	v_exp_f32_e32 v93, v93
	v_add_f32_e32 v160, v89, v160
	v_exp_f32_e32 v94, v94
	v_add_f32_e32 v160, v90, v160
	v_exp_f32_e32 v95, v95
	v_add_f32_e32 v160, v91, v160
	v_add_f32_e32 v160, v92, v160
	v_add_f32_e32 v160, v93, v160
	v_add_f32_e32 v160, v94, v160
	v_add_f32_e32 v160, v95, v160
	v_mov_b32_e32 v161, v160
	v_cvt_pk_bf16_f32 v172, v96, v97
	v_cvt_pk_bf16_f32 v173, v98, v99
	v_permlane32_swap_b32_e32 v160, v161
	v_add_f32_e32 v160, v160, v161
	v_add_f32_e32 v204, v204, v160
	v_cvt_pk_bf16_f32 v174, v100, v101
	v_cvt_pk_bf16_f32 v175, v102, v103
	v_cvt_pk_bf16_f32 v168, v104, v105
	v_cvt_pk_bf16_f32 v169, v106, v107
	v_cvt_pk_bf16_f32 v170, v108, v109
	v_cvt_pk_bf16_f32 v171, v110, v111
	v_cvt_pk_bf16_f32 v164, v80, v81
	v_cvt_pk_bf16_f32 v165, v82, v83
	v_cvt_pk_bf16_f32 v166, v84, v85
	v_cvt_pk_bf16_f32 v167, v86, v87
	v_cvt_pk_bf16_f32 v160, v88, v89
	v_cvt_pk_bf16_f32 v161, v90, v91
	v_cvt_pk_bf16_f32 v162, v92, v93
	v_cvt_pk_bf16_f32 v163, v94, v95
	s_mul_i32 s47, s26, 0x6000
	s_addk_i32 s93, 0xc000
	s_cmp_lg_u32 s26, 0
	s_cselect_b32 s46, s93, 0x8000
	v_add_u32_e32 v227, s46, v202
	v_add_u32_e32 v207, s47, v185
	v_add_u32_e32 v224, s47, v187
	v_add_u32_e32 v225, s47, v205
	v_add_u32_e32 v226, s47, v206
	s_waitcnt lgkmcnt(0)
	ds_read_b64_tr_b16 v[208:209], v227 offset:0
	ds_read_b64_tr_b16 v[210:211], v227 offset:2048
	ds_read_b64_tr_b16 v[212:213], v227 offset:512
	ds_read_b64_tr_b16 v[214:215], v227 offset:2560
	ds_read_b64_tr_b16 v[216:217], v227 offset:1024
	ds_read_b64_tr_b16 v[218:219], v227 offset:3072
	ds_read_b64_tr_b16 v[220:221], v227 offset:1536
	ds_read_b64_tr_b16 v[222:223], v227 offset:3584
	s_barrier
; #define SBAR() __builtin_amdgcn_sched_barrier(0)
; #define LWN1(a) do { if constexpr (NW == 0) LW1(0, a); else if constexpr (NW == 1) LW1(1, a); else if constexpr (NW == 2) LW1(2, a); else if constexpr (NW == 3) LW1(3, a); else if constexpr (NW == 4) LW1(4, a); else if constexpr (NW == 5) LW1(5, a); else LW1(6, a); } while (0)
; #define LWN2(a, b) do { if constexpr (NW == 0) LW2(0, a, b); else if constexpr (NW == 1) LW2(1, a, b); else if constexpr (NW == 2) LW2(2, a, b); else if constexpr (NW == 3) LW2(3, a, b); else if constexpr (NW == 4) LW2(4, a, b); else if constexpr (NW == 5) LW2(5, a, b); else LW2(6, a, b); } while (0)
; template <int DQK, bool HASQK, bool HASPV, int J> ...
;     constexpr int NQS = HASQK ? 2 * (DQK / 16) : 0, NS = NQS + (HASPV ? 16 : 0);
;     if constexpr (J < NS) {
;         constexpr int rd1 = (J + 1 < NS) ? ((J + 1 < NQS) ? 1 : 2) : 0, rd2 = (J + 2 < NS) ? ((J + 2 < NQS) ? 1 : 2) : 0, rd3 = (J + 3 < NS) ? ((J + 3 < NQS) ? 1 : 2) : 0, NW = rd1 + rd2 + rd3;
;     ...
;         if constexpr (J < NQS) { constexpr int d0 = J >> 1, h = J & 1;
;             LWN1(kf[d0][h]); SBAR();
;             if constexpr (h == 0) p0 = __builtin_amdgcn_mfma_f32_32x32x16_bf16(kf[d0][0], qr[d0], (d0 == 0) ? negm : p0, 0, 0, 0);
;             else p1 = __builtin_amdgcn_mfma_f32_32x32x16_bf16(kf[d0][1], qr[d0], (d0 == 0) ? negm : p1, 0, 0, 0);
;         } else { constexpr int q = J - NQS, g = q >> 2, d = q & 3;
;             LWN2(vf[g][2 * d], vf[g][2 * d + 1]); SBAR();
;             o[d] = __builtin_amdgcn_mfma_f32_32x32x16_bf16(pa[g], (bf16x8){vf[g][2 * d][0], vf[g][2 * d][1], vf[g][2 * d][2], vf[g][2 * d][3], vf[g][2 * d + 1][0], vf[g][2 * d + 1][1], vf[g][2 * d + 1][2], vf[g][2 * d + 1][3]}, o[d], 0, 0, 0);
;         }
;     ...
;         SBAR();
;         slot_read<DQK, HASQK, HASPV, J + 4>(kf, vf, ka_, vb_);
;         SBAR();
;         slot_run<DQK, HASQK, HASPV, J + 1>(kf, vf, ka_, vb_, qr, p0, p1, negm, o, pa);
; template <int DQK, bool HASQK, bool HASPV>
; __device__ __forceinline__ void seg_m2(const int (&ka_)[4], int vb_, const bf16x8* qr, f32x16& p0, f32x16& p1, const float nm, f32x16 (&o)[4], bf16x8 pa0, bf16x8 pa1, bf16x8 pa2, bf16x8 pa3) {
;     ...
;     f32x16 negm;
; #pragma unroll
;     for (int r = 0; r < 16; ++r) negm[r] = nm;
;     asm volatile("" : "+v"(negm));
	s_waitcnt lgkmcnt(6)
	v_mfma_f32_32x32x16_bf16 v[64:79], v[172:175], v[208:211], v[64:79]
	ds_read_b64_tr_b16 v[208:209], v227 offset:4096
	ds_read_b64_tr_b16 v[210:211], v227 offset:6144
	v_xor_b32_e32 v80, 0x80000000, v203
	v_mov_b32_e32 v81, v80
	s_waitcnt lgkmcnt(6)
	v_mfma_f32_32x32x16_bf16 v[48:63], v[172:175], v[212:215], v[48:63]
	ds_read_b64_tr_b16 v[212:213], v227 offset:4608
	ds_read_b64_tr_b16 v[214:215], v227 offset:6656
	v_mov_b32_e32 v82, v80
	s_waitcnt lgkmcnt(6)
	v_mfma_f32_32x32x16_bf16 v[32:47], v[172:175], v[216:219], v[32:47]
	ds_read_b64_tr_b16 v[216:217], v227 offset:5120
	ds_read_b64_tr_b16 v[218:219], v227 offset:7168
	v_mov_b32_e32 v83, v80
	s_waitcnt lgkmcnt(6)
	v_mfma_f32_32x32x16_bf16 v[16:31], v[172:175], v[220:223], v[16:31]
	ds_read_b64_tr_b16 v[220:221], v227 offset:5632
	ds_read_b64_tr_b16 v[222:223], v227 offset:7680
	v_mov_b32_e32 v84, v80
	s_waitcnt lgkmcnt(6)
	v_mfma_f32_32x32x16_bf16 v[64:79], v[168:171], v[208:211], v[64:79]
	ds_read_b64_tr_b16 v[208:209], v227 offset:8192
	ds_read_b64_tr_b16 v[210:211], v227 offset:10240
	v_mov_b32_e32 v85, v80
	s_waitcnt lgkmcnt(6)
	v_mfma_f32_32x32x16_bf16 v[48:63], v[168:171], v[212:215], v[48:63]
	ds_read_b64_tr_b16 v[212:213], v227 offset:8704
	ds_read_b64_tr_b16 v[214:215], v227 offset:10752
	v_mov_b32_e32 v86, v80
	s_waitcnt lgkmcnt(6)
	v_mfma_f32_32x32x16_bf16 v[32:47], v[168:171], v[216:219], v[32:47]
	ds_read_b64_tr_b16 v[216:217], v227 offset:9216
	ds_read_b64_tr_b16 v[218:219], v227 offset:11264
	v_mov_b32_e32 v87, v80
	s_waitcnt lgkmcnt(6)
	v_mfma_f32_32x32x16_bf16 v[16:31], v[168:171], v[220:223], v[16:31]
	ds_read_b64_tr_b16 v[220:221], v227 offset:9728
	ds_read_b64_tr_b16 v[222:223], v227 offset:11776
	v_mov_b32_e32 v88, v80
	s_waitcnt lgkmcnt(6)
	v_mfma_f32_32x32x16_bf16 v[64:79], v[164:167], v[208:211], v[64:79]
	ds_read_b64_tr_b16 v[208:209], v227 offset:12288
	ds_read_b64_tr_b16 v[210:211], v227 offset:14336
	v_mov_b32_e32 v89, v80
	s_waitcnt lgkmcnt(6)
	v_mfma_f32_32x32x16_bf16 v[48:63], v[164:167], v[212:215], v[48:63]
	ds_read_b64_tr_b16 v[212:213], v227 offset:12800
	ds_read_b64_tr_b16 v[214:215], v227 offset:14848
	v_mov_b32_e32 v90, v80
	s_waitcnt lgkmcnt(6)
	v_mfma_f32_32x32x16_bf16 v[32:47], v[164:167], v[216:219], v[32:47]
	ds_read_b64_tr_b16 v[216:217], v227 offset:13312
	ds_read_b64_tr_b16 v[218:219], v227 offset:15360
	v_mov_b32_e32 v91, v80
	s_waitcnt lgkmcnt(6)
	v_mfma_f32_32x32x16_bf16 v[16:31], v[164:167], v[220:223], v[16:31]
	ds_read_b64_tr_b16 v[220:221], v227 offset:13824
	ds_read_b64_tr_b16 v[222:223], v227 offset:15872
	v_mov_b32_e32 v92, v80
	s_waitcnt lgkmcnt(6)
	v_mfma_f32_32x32x16_bf16 v[64:79], v[160:163], v[208:211], v[64:79]
	ds_read_b128 v[208:211], v207 offset:0
	v_mov_b32_e32 v93, v80
	s_waitcnt lgkmcnt(5)
	v_mfma_f32_32x32x16_bf16 v[48:63], v[160:163], v[212:215], v[48:63]
	ds_read_b128 v[212:215], v207 offset:12288
	v_mov_b32_e32 v94, v80
	s_waitcnt lgkmcnt(4)
	v_mfma_f32_32x32x16_bf16 v[32:47], v[160:163], v[216:219], v[32:47]
	ds_read_b128 v[216:219], v224 offset:0
	v_mov_b32_e32 v95, v80
	s_waitcnt lgkmcnt(3)
	v_mfma_f32_32x32x16_bf16 v[16:31], v[160:163], v[220:223], v[16:31]
	ds_read_b128 v[220:223], v224 offset:12288
	s_waitcnt lgkmcnt(3)
	v_mfma_f32_32x32x16_bf16 v[96:111], v[208:211], v[112:115], v[80:95]
	ds_read_b128 v[208:211], v225 offset:0
	s_waitcnt lgkmcnt(3)
	v_mfma_f32_32x32x16_bf16 v[80:95], v[212:215], v[112:115], v[80:95]
	ds_read_b128 v[212:215], v225 offset:12288
	s_waitcnt lgkmcnt(3)
	v_mfma_f32_32x32x16_bf16 v[96:111], v[216:219], v[116:119], v[96:111]
	ds_read_b128 v[216:219], v226 offset:0
	s_waitcnt lgkmcnt(3)
	v_mfma_f32_32x32x16_bf16 v[80:95], v[220:223], v[116:119], v[80:95]
	ds_read_b128 v[220:223], v226 offset:12288
	s_waitcnt lgkmcnt(3)
	v_mfma_f32_32x32x16_bf16 v[96:111], v[208:211], v[120:123], v[96:111]
	ds_read_b128 v[208:211], v207 offset:128
	s_waitcnt lgkmcnt(3)
	v_mfma_f32_32x32x16_bf16 v[80:95], v[212:215], v[120:123], v[80:95]
	ds_read_b128 v[212:215], v207 offset:12416
	s_waitcnt lgkmcnt(3)
	v_mfma_f32_32x32x16_bf16 v[96:111], v[216:219], v[124:127], v[96:111]
	ds_read_b128 v[216:219], v224 offset:128
	s_waitcnt lgkmcnt(3)
	v_mfma_f32_32x32x16_bf16 v[80:95], v[220:223], v[124:127], v[80:95]
	ds_read_b128 v[220:223], v224 offset:12416
	s_waitcnt lgkmcnt(3)
	v_mfma_f32_32x32x16_bf16 v[96:111], v[208:211], v[128:131], v[96:111]
	ds_read_b128 v[208:211], v225 offset:128
	s_waitcnt lgkmcnt(3)
	v_mfma_f32_32x32x16_bf16 v[80:95], v[212:215], v[128:131], v[80:95]
	ds_read_b128 v[212:215], v225 offset:12416
	s_waitcnt lgkmcnt(3)
	v_mfma_f32_32x32x16_bf16 v[96:111], v[216:219], v[132:135], v[96:111]
	ds_read_b128 v[216:219], v226 offset:128
	s_waitcnt lgkmcnt(3)
	v_mfma_f32_32x32x16_bf16 v[80:95], v[220:223], v[132:135], v[80:95]
	ds_read_b128 v[220:223], v226 offset:12416
	s_waitcnt lgkmcnt(3)
	v_mfma_f32_32x32x16_bf16 v[96:111], v[208:211], v[136:139], v[96:111]
	ds_read_b128 v[208:211], v207 offset:256
	s_waitcnt lgkmcnt(3)
	v_mfma_f32_32x32x16_bf16 v[80:95], v[212:215], v[136:139], v[80:95]
	ds_read_b128 v[212:215], v207 offset:12544
	s_waitcnt lgkmcnt(3)
	v_mfma_f32_32x32x16_bf16 v[96:111], v[216:219], v[140:143], v[96:111]
	ds_read_b128 v[216:219], v224 offset:256
	s_waitcnt lgkmcnt(3)
	v_mfma_f32_32x32x16_bf16 v[80:95], v[220:223], v[140:143], v[80:95]
	ds_read_b128 v[220:223], v224 offset:12544
	s_waitcnt lgkmcnt(3)
	v_mfma_f32_32x32x16_bf16 v[96:111], v[208:211], v[144:147], v[96:111]
	ds_read_b128 v[208:211], v225 offset:256
	s_waitcnt lgkmcnt(3)
	v_mfma_f32_32x32x16_bf16 v[80:95], v[212:215], v[144:147], v[80:95]
	ds_read_b128 v[212:215], v225 offset:12544
	s_waitcnt lgkmcnt(3)
	v_mfma_f32_32x32x16_bf16 v[96:111], v[216:219], v[148:151], v[96:111]
	ds_read_b128 v[216:219], v226 offset:256
	s_waitcnt lgkmcnt(3)
	v_mfma_f32_32x32x16_bf16 v[80:95], v[220:223], v[148:151], v[80:95]
	ds_read_b128 v[220:223], v226 offset:12544
	s_waitcnt lgkmcnt(3)
	v_mfma_f32_32x32x16_bf16 v[96:111], v[208:211], v[152:155], v[96:111]
	s_waitcnt lgkmcnt(2)
	v_mfma_f32_32x32x16_bf16 v[80:95], v[212:215], v[152:155], v[80:95]
	s_waitcnt lgkmcnt(1)
	v_mfma_f32_32x32x16_bf16 v[96:111], v[216:219], v[156:159], v[96:111]
	s_waitcnt lgkmcnt(0)
	v_mfma_f32_32x32x16_bf16 v[80:95], v[220:223], v[156:159], v[80:95]
	s_waitcnt vmcnt(0)
	s_waitcnt lgkmcnt(0)
	s_barrier
	s_add_u32 s44, s44, 0x18000
	s_addc_u32 s45, s45, 0
	v_lshl_add_u64 v[194:195], v[194:195], 0, s[28:29]
	s_cmp_eq_u32 s44, 0xbe8000
	v_lshl_add_u64 v[196:197], v[196:197], 0, s[28:29]
	s_cbranch_scc1 .LBB0_616
